# DeltaNet prep: gate inputs (alpha, beta, a_log, dt_bias) loaded one item ahead next to the raw-row DMA instead of inside the gate stage
# speedup vs baseline: 1.0008x; 1.0008x over previous
; __device__ __forceinline__ float bf2f(bf16_t v) { return __uint_as_float(((unsigned)v) << 16); }
; __device__ __forceinline__ float fexp(float x) { return __builtin_amdgcn_exp2f(x * 1.4426950408889634f); }
; __device__ __forceinline__ float sigmoidf_(float x) { return __builtin_amdgcn_rcpf(1.f + fexp(-x)); }
; __device__ __forceinline__ float softplusf_(float x) { return x > 20.f ? x : 0.6931471805599453f * __builtin_amdgcn_logf(1.f + fexp(x)); }
; __device__ void phase_gdn_prep(const Params& p, int l, char* smem, int vb, int nvb, int pend, int oz) {
;     ...
;         if (tid < 128) {
;             const int dd = tid >> 6, t = tid & 63;
;             const size_t row = rowbase + t0 + t;
;             const float alpha = bf2f(U[row * LDU + C_GA + dd * 4 + h]);
;             const float beta = bf2f(U[row * LDU + C_GB + dd * 4 + h]);
;             gl[tid] = -1.4426950408889634f * fexp(p.in[I_GALOG][(l * 2 + dd) * 4 + h]) * softplusf_(alpha + p.in[I_GDT][(l * 2 + dd) * 4 + h]);
;             bl[tid] = sigmoidf_(beta);
;         }
.LBB0_521:
	s_or_b64 exec, exec, s[0:1]
	v_and_b32_e32 v60, 63, v8
	v_cmp_gt_u32_e32 vcc, s59, v9
	s_and_saveexec_b64 s[0:1], vcc
	s_cbranch_execz .LBB0_523
	s_ashr_i32 s25, s25, 5
	s_add_i32 s26, s25, s26
	s_ashr_i32 s27, s26, 31
	s_lshl_b64 s[38:39], s[26:27], 8
	s_add_u32 s25, s38, 0x4000
	s_addc_u32 s31, s39, 0
	s_lshl_b64 s[26:27], s[26:27], 11
	s_and_b64 s[28:29], s[28:29], exec
	s_cselect_b32 s27, s31, s27
	s_cselect_b32 s26, s25, s26
	s_ashr_i32 s25, s24, 31
	v_or_b32_e32 v4, s24, v60
	v_mov_b32_e32 v5, s25
	v_lshl_add_u64 v[4:5], v[4:5], 0, s[26:27]
	v_mov_b64_e32 v[6:7], s[34:35]
	v_mad_u64_u32 v[6:7], s[24:25], v4, s92, v[6:7]
	v_mad_i32_i24 v7, v5, s92, v7
	v_lshlrev_b32_e32 v2, 3, v11
	s_lshl_b32 s96, s3, 1
	v_lshl_add_u64 v[4:5], v[6:7], 0, v[2:3]
	v_lshl_add_u64 v[4:5], v[4:5], 0, s[96:97]
	v_add_co_u32_e32 v4, vcc, s22, v4
	s_or_b32 s3, s3, s8
	s_nop 0
	v_addc_co_u32_e32 v5, vcc, 0, v5, vcc
	v_readlane_b32 s40, v253, 18
	v_readlane_b32 s44, v253, 22
	v_readlane_b32 s45, v253, 23
	v_readlane_b32 s46, v253, 24
	v_readlane_b32 s47, v253, 25
	v_readlane_b32 s41, v253, 19
	v_readlane_b32 s42, v253, 20
	v_readlane_b32 s43, v253, 21
	v_readlane_b32 s48, v253, 26
	v_readlane_b32 s49, v253, 27
	v_readlane_b32 s50, v253, 28
	v_readlane_b32 s51, v253, 29
	v_readlane_b32 s52, v253, 30
	v_readlane_b32 s53, v253, 31
	v_readlane_b32 s54, v253, 32
	v_readlane_b32 s55, v253, 33
	v_lshl_or_b32 v4, v11, 2, s3
	v_ashrrev_i32_e32 v5, 31, v4
	v_lshlrev_b64 v[4:5], 2, v[4:5]
	v_lshl_add_u64 v[6:7], s[44:45], 0, v[4:5]
	v_lshl_add_u64 v[4:5], s[46:47], 0, v[4:5]
	s_mov_b32 s3, 0x41a00000
	s_waitcnt vmcnt(3)
	v_lshlrev_b32_e32 v2, 16, v242
	s_waitcnt vmcnt(2)
	v_lshlrev_b32_e32 v12, 16, v243
	s_waitcnt vmcnt(1)
	v_add_f32_e32 v2, v244, v2
	v_mul_f32_e32 v4, 0x3fb8aa3b, v2
	v_exp_f32_e32 v4, v4
	v_cmp_lt_f32_e32 vcc, s3, v2
	s_waitcnt vmcnt(0)
	v_mul_f32_e32 v6, 0x3fb8aa3b, v245
	v_exp_f32_e32 v6, v6
	v_add_f32_e32 v4, 1.0, v4
	v_log_f32_e32 v4, v4
	v_mul_f32_e32 v6, 0xbfb8aa3b, v6
	v_mul_f32_e32 v4, 0x3f317218, v4
	v_cndmask_b32_e32 v2, v4, v2, vcc
	v_mul_f32_e32 v4, 0xbfb8aa3b, v12
	v_exp_f32_e32 v4, v4
	v_mul_f32_e32 v2, v6, v2
	v_add_f32_e32 v4, 1.0, v4
	v_rcp_f32_e32 v4, v4
	ds_write2st64_b32 v10, v2, v4 offset0:220 offset1:222

; __device__ __forceinline__ float bf2f(bf16_t v) { return __uint_as_float(((unsigned)v) << 16); }
; __device__ __forceinline__ float fexp(float x) { return __builtin_amdgcn_exp2f(x * 1.4426950408889634f); }
; __device__ __forceinline__ float softplusf_(float x) { return x > 20.f ? x : 0.6931471805599453f * __builtin_amdgcn_logf(1.f + fexp(x)); }
; __device__ void phase_gdn_prep(const Params& p, int l, char* smem, int vb, int nvb, int pend, int oz) {
;     ...
;             const float alpha = bf2f(U[row * LDU + C_GA + dd * 4 + h]);
;             const float beta = bf2f(U[row * LDU + C_GB + dd * 4 + h]);
;             gl[tid] = -1.4426950408889634f * fexp(p.in[I_GALOG][(l * 2 + dd) * 4 + h]) * softplusf_(alpha + p.in[I_GDT][(l * 2 + dd) * 4 + h]);
.LBB0_550:
	s_mul_hi_i32 s2, s36, 0x38e38e39
	s_ashr_i32 s3, s2, 5
	s_lshr_b32 s25, s2, 31
	s_ashr_i32 s2, s2, 3
	s_add_i32 s38, s2, s25
	s_mul_i32 s2, s38, 36
	s_add_i32 s24, s3, s25
	s_sub_i32 s2, s36, s2
	s_cmp_lt_i32 s2, 4
	s_cselect_b64 s[26:27], -1, 0
	s_lshl_b32 s25, s2, 6
	s_add_i32 s28, s25, 0xffffff00
	s_and_b64 s[2:3], s[26:27], exec
	s_cselect_b32 s2, s25, s28
	s_cselect_b32 s3, 0x100, s30
	s_ashr_i32 s25, s24, 31
	s_lshl_b64 s[28:29], s[24:25], 8
	s_add_u32 s28, s28, 0x4000
	s_addc_u32 s29, s29, 0
	s_lshl_b64 s[24:25], s[24:25], 11
	s_and_b64 s[26:27], s[26:27], exec
	s_cselect_b32 s29, s29, s25
	s_cselect_b32 s28, s28, s24
	v_readfirstlane_b32 s24, v1
	s_lshr_b32 s24, s24, 6
	s_cmp_gt_u32 s24, 1
	s_cbranch_scc1 .Lgp_pf_skip
	s_and_b32 s25, s38, 3
	v_add_u32_e32 v242, s2, v236
	v_mov_b32_e32 v243, 0
	v_lshl_add_u64 v[242:243], s[28:29], 0, v[242:243]
	v_mov_b64_e32 v[244:245], s[34:35]
	v_mad_u64_u32 v[244:245], vcc, v242, s92, v[244:245]
	v_mad_i32_i24 v245, v243, s92, v245
	s_lshl_b32 s6, s24, 3
	s_lshl_b32 s7, s25, 1
	s_add_i32 s6, s6, s7
	s_add_u32 s6, s6, s22
	s_mov_b32 s7, 0
	v_lshl_add_u64 v[244:245], v[244:245], 0, s[6:7]
	global_load_ushort v242, v[244:245], off offset:2560
	global_load_ushort v243, v[244:245], off offset:2576
	s_lshl_b32 s6, s24, 2
	s_or_b32 s6, s6, s25
	s_or_b32 s6, s6, s8
	s_lshl_b32 s6, s6, 2
	v_mov_b32_e32 v240, s6
	v_readlane_b32 s24, v253, 24
	v_readlane_b32 s25, v253, 25
	s_nop 4
	global_load_dword v244, v240, s[24:25]
	v_readlane_b32 s24, v253, 22
	v_readlane_b32 s25, v253, 23
	s_nop 4
	global_load_dword v245, v240, s[24:25]
.Lgp_pf_skip:
	s_add_i32 s24, s2, -2
	v_add_u32_e32 v2, s24, v164
	v_mov_b32_e32 v8, s2
	v_cmp_gt_u32_e32 vcc, s3, v2
	s_lshl_b32 s25, s38, 6
	v_readfirstlane_b32 s31, v1
	v_cndmask_b32_e32 v4, v8, v2, vcc
	v_ashrrev_i32_e32 v5, 31, v4
	v_lshl_add_u64 v[4:5], s[28:29], 0, v[4:5]
	s_and_b32 s25, s25, 0xc0
	v_mad_u64_u32 v[6:7], s[26:27], v4, s92, v[104:105]
	v_mad_i32_i24 v7, v5, s92, v7
	s_lshl_b32 s96, s25, 1
	s_lshl_b32 s25, s31, 4
	v_lshl_add_u64 v[4:5], v[6:7], 0, s[96:97]
	v_mov_b32_e32 v119, v3
	s_and_b32 s25, s25, 0xfffffc00
	v_lshl_add_u64 v[4:5], v[4:5], 0, v[118:119]
	s_mov_b64 s[6:7], 0x400
	s_add_i32 s25, s81, s25
	v_add_u32_e32 v2, s24, v165
	v_lshl_add_u64 v[4:5], v[4:5], 0, s[6:7]
	s_mov_b32 m0, s25
	v_cmp_gt_u32_e32 vcc, s3, v2
	global_load_lds_dwordx4 v[4:5], off
	s_nop 0
	v_cndmask_b32_e32 v4, v8, v2, vcc
	v_ashrrev_i32_e32 v5, 31, v4
	v_lshl_add_u64 v[4:5], s[28:29], 0, v[4:5]
	v_mad_u64_u32 v[6:7], s[26:27], v4, s92, v[106:107]
	v_mad_i32_i24 v7, v5, s92, v7
	v_lshl_add_u64 v[4:5], v[6:7], 0, s[96:97]
	v_mov_b32_e32 v121, v3
	v_lshl_add_u64 v[4:5], v[4:5], 0, v[120:121]
	v_add_u32_e32 v2, s24, v166
	v_lshl_add_u64 v[4:5], v[4:5], 0, s[6:7]
	s_add_i32 m0, s25, 0x1000
	v_cmp_gt_u32_e32 vcc, s3, v2
	global_load_lds_dwordx4 v[4:5], off
	s_nop 0
	v_cndmask_b32_e32 v4, v8, v2, vcc
	v_ashrrev_i32_e32 v5, 31, v4
	v_lshl_add_u64 v[4:5], s[28:29], 0, v[4:5]
	v_mad_u64_u32 v[6:7], s[26:27], v4, s92, v[108:109]
	v_mad_i32_i24 v7, v5, s92, v7
	v_lshl_add_u64 v[4:5], v[6:7], 0, s[96:97]
	v_mov_b32_e32 v123, v3
	v_lshl_add_u64 v[4:5], v[4:5], 0, v[122:123]
	v_add_u32_e32 v2, s24, v167
	v_lshl_add_u64 v[4:5], v[4:5], 0, s[6:7]
	s_add_i32 m0, s25, 0x2000
	v_cmp_gt_u32_e32 vcc, s3, v2
	global_load_lds_dwordx4 v[4:5], off
	s_nop 0
	v_cndmask_b32_e32 v4, v8, v2, vcc
	v_ashrrev_i32_e32 v5, 31, v4
	v_lshl_add_u64 v[4:5], s[28:29], 0, v[4:5]
	v_mad_u64_u32 v[6:7], s[26:27], v4, s92, v[110:111]
	v_mad_i32_i24 v7, v5, s92, v7
	v_lshl_add_u64 v[4:5], v[6:7], 0, s[96:97]
	v_mov_b32_e32 v125, v3
	v_lshl_add_u64 v[4:5], v[4:5], 0, v[124:125]
	v_add_u32_e32 v2, s24, v168
	v_lshl_add_u64 v[4:5], v[4:5], 0, s[6:7]
	s_add_i32 m0, s25, 0x3000
	v_cmp_gt_u32_e32 vcc, s3, v2
	global_load_lds_dwordx4 v[4:5], off
	s_nop 0
	v_cndmask_b32_e32 v4, v8, v2, vcc
	v_ashrrev_i32_e32 v5, 31, v4
	v_lshl_add_u64 v[4:5], s[28:29], 0, v[4:5]
	v_mad_u64_u32 v[6:7], s[26:27], v4, s92, v[112:113]
	v_mad_i32_i24 v7, v5, s92, v7
	v_lshl_add_u64 v[4:5], v[6:7], 0, s[96:97]
	v_mov_b32_e32 v127, v3
	v_lshl_add_u64 v[4:5], v[4:5], 0, v[126:127]
	v_add_u32_e32 v2, s24, v169
	v_lshl_add_u64 v[4:5], v[4:5], 0, s[6:7]
	s_add_i32 m0, s25, 0x4000
	v_cmp_gt_u32_e32 vcc, s3, v2
	global_load_lds_dwordx4 v[4:5], off
	s_nop 0
	v_cndmask_b32_e32 v4, v8, v2, vcc
	v_ashrrev_i32_e32 v5, 31, v4
	v_lshl_add_u64 v[4:5], s[28:29], 0, v[4:5]
	v_mad_u64_u32 v[6:7], s[26:27], v4, s92, v[114:115]
	v_mad_i32_i24 v7, v5, s92, v7
	v_lshl_add_u64 v[4:5], v[6:7], 0, s[96:97]
	v_mov_b32_e32 v129, v3
	v_lshl_add_u64 v[4:5], v[4:5], 0, v[128:129]
	v_lshl_add_u64 v[4:5], v[4:5], 0, s[6:7]
	s_add_i32 m0, s25, 0x5000
	s_mov_b64 s[4:5], 0x400
	global_load_lds_dwordx4 v[4:5], off
	s_and_saveexec_b64 s[38:39], s[18:19]
	s_cbranch_execz .LBB0_552
	v_add_u32_e32 v2, s24, v170
	v_mov_b32_e32 v4, s2
	v_cmp_gt_u32_e32 vcc, s3, v2
	v_mov_b32_e32 v131, v3
	s_add_i32 m0, s25, 0x6000
	v_cndmask_b32_e32 v4, v4, v2, vcc
	v_ashrrev_i32_e32 v5, 31, v4
	v_lshl_add_u64 v[4:5], s[28:29], 0, v[4:5]
	v_mad_u64_u32 v[6:7], s[2:3], v4, s92, v[116:117]
	v_mov_b32_e32 v2, v7
	v_mad_u64_u32 v[4:5], s[2:3], v5, s92, v[2:3]
	v_mov_b32_e32 v7, v4
	v_lshl_add_u64 v[4:5], v[6:7], 0, s[96:97]
	v_lshl_add_u64 v[4:5], v[4:5], 0, v[130:131]
	v_lshl_add_u64 v[4:5], v[4:5], 0, s[4:5]
	global_load_lds_dwordx4 v[4:5], off
